# speedup vs baseline: 1.0297x; 1.0297x over previous
_Z16sum_layer_kernelPKfS0_Pf:
	s_load_dwordx4 s[4:7], s[0:1], 0x0
	s_load_dwordx2 s[8:9], s[0:1], 0x10
	v_lshrrev_b32_e32 v42, 6, v0
	v_bfe_u32 v41, v0, 5, 1
	v_and_b32_e32 v40, 31, v0
	v_readfirstlane_b32 s23, v42
	v_and_b32_e32 v43, 7, v0
	v_bfe_u32 v44, v0, 3, 3
	s_lshl_b32 s3, s2, 12
	s_lshl_b32 s19, s2, 7
	s_lshl_b32 s23, s23, 12
	v_lshlrev_b32_e32 v1, 11, v41
	v_lshl_or_b32 v1, v40, 2, v1
	s_mov_b32 m0, s23
	v_lshrrev_b32_e32 v46, 1, v44
	v_xor_b32_e32 v46, v43, v46
	v_lshlrev_b32_e32 v46, 4, v46
	v_lshl_add_u32 v35, v44, 16, v46
	v_lshl_add_u32 v35, v42, 21, v35
	v_add_u32_e32 v35, s19, v35
	v_xor_b32_e32 v86, 64, v35
	s_mov_b32 s20, 0x7fc00
	s_mov_b32 s21, 0xff800
	s_mov_b32 s22, 0x17f400
	s_mov_b32 s14, 0x200000
	s_mov_b32 s15, 0x20000
	v_and_b32_e32 v45, 63, v0
	v_lshlrev_b32_e32 v37, 4, v45
	s_add_u32 s54, s23, 0x4000
	s_waitcnt lgkmcnt(0)
	s_mov_b32 s12, s6
	s_and_b32 s13, s7, 0xffff
	s_and_b32 s5, s5, 0xffff
	s_mov_b32 s6, 0x800000
	s_mov_b32 s7, s15
	s_mov_b32 m0, s54
	s_nop 0
	buffer_load_dwordx4 v37, s[12:15], s3 offen nt lds
	buffer_load_dwordx4 v37, s[12:15], s3 offen offset:1024 nt lds
	buffer_load_dwordx4 v37, s[12:15], s3 offen offset:2048 nt lds
	buffer_load_dwordx4 v37, s[12:15], s3 offen offset:3072 nt lds
	s_mov_b32 m0, s23
	s_nop 0
	buffer_load_dwordx4 v35, s[4:7], 0 offen nt lds
	buffer_load_dwordx4 v86, s[4:7], s20 offen offset:1024 nt lds
	buffer_load_dwordx4 v35, s[4:7], s21 offen offset:2048 nt lds
	buffer_load_dwordx4 v86, s[4:7], s22 offen offset:3072 nt lds
	v_and_b32_e32 v45, 63, v0
	v_lshlrev_b32_e32 v36, 2, v40
	v_lshl_add_u32 v36, v41, 18, v36
	v_lshl_add_u32 v36, v42, 21, v36
	v_add_u32_e32 v36, s19, v36
	v_bfe_u32 v47, v40, 1, 3
	v_lshlrev_b32_e32 v39, 2, v41
	v_xor_b32_e32 v39, v39, v47
	v_lshlrev_b32_e32 v39, 4, v39
	v_lshl_add_u32 v39, v40, 7, v39
	v_lshl_add_u32 v39, v42, 12, v39
	v_xor_b32_e32 v81, 16, v39
	v_xor_b32_e32 v82, 32, v39
	v_xor_b32_e32 v83, 48, v39
	v_cmp_gt_u32_e32 vcc, 32, v45
	v_mov_b32_e32 v34, 0xc1600000
	v_mov_b32_e32 v84, 0x3fb8aa3b
	v_mov_b32_e32 v85, 0x3f317218
	s_lshl_b32 s24, 1, 16
	s_lshl_b32 s25, 2, 16
	s_lshl_b32 s26, 3, 16
	s_lshl_b32 s27, 8, 16
	s_lshl_b32 s28, 9, 16
	s_lshl_b32 s29, 10, 16
	s_lshl_b32 s30, 11, 16
	s_lshl_b32 s31, 16, 16
	s_lshl_b32 s32, 17, 16
	s_lshl_b32 s33, 18, 16
	s_lshl_b32 s34, 19, 16
	s_lshl_b32 s35, 24, 16
	s_lshl_b32 s36, 25, 16
	s_lshl_b32 s37, 26, 16
	s_lshl_b32 s38, 27, 16
	s_and_b32 s9, s9, 0xffff
	s_mov_b32 s10, s6
	s_mov_b32 s11, s15
	v_lshl_add_u32 v38, v42, 12, v1
	v_add_u32_e32 v38, 0x4000, v38
	v_add_u32_e32 v87, 0x400, v38
	s_waitcnt vmcnt(4)
	ds_read2_b32 v[18:19], v38 offset0:0 offset1:32
	ds_read2_b32 v[20:21], v38 offset0:64 offset1:96
	ds_read2_b32 v[22:23], v38 offset0:128 offset1:160
	ds_read2_b32 v[24:25], v38 offset0:192 offset1:224
	ds_read2_b32 v[26:27], v87 offset0:0 offset1:32
	ds_read2_b32 v[28:29], v87 offset0:64 offset1:96
	ds_read2_b32 v[30:31], v87 offset0:128 offset1:160
	ds_read2_b32 v[32:33], v87 offset0:192 offset1:224
	s_waitcnt lgkmcnt(0)
	v_max3_f32 v48, v18, v19, v20
	v_max3_f32 v50, v21, v22, v23
	v_max3_f32 v48, v48, v24, v25
	v_max3_f32 v50, v50, v26, v27
	v_max3_f32 v48, v48, v28, v29
	v_max3_f32 v50, v50, v30, v31
	v_max3_f32 v48, v48, v32, v33
	v_max_f32_e32 v48, v48, v50
	v_mov_b32_e32 v50, v48
	s_nop 1
	v_permlane32_swap_b32_e32 v48, v50
	v_max_f32_e32 v48, v48, v50
	v_fmamk_f32 v48, v48, 0x3fb8aa3b, v34
	v_pk_fma_f32 v[18:19], v[18:19], v[84:85], v[48:49] op_sel_hi:[1,0,0] neg_lo:[0,0,1] neg_hi:[0,0,1]
	v_exp_f32_e32 v18, v18
	v_exp_f32_e32 v19, v19
	v_pk_fma_f32 v[20:21], v[20:21], v[84:85], v[48:49] op_sel_hi:[1,0,0] neg_lo:[0,0,1] neg_hi:[0,0,1]
	v_exp_f32_e32 v20, v20
	v_exp_f32_e32 v21, v21
	v_pk_fma_f32 v[22:23], v[22:23], v[84:85], v[48:49] op_sel_hi:[1,0,0] neg_lo:[0,0,1] neg_hi:[0,0,1]
	v_exp_f32_e32 v22, v22
	v_exp_f32_e32 v23, v23
	v_pk_fma_f32 v[24:25], v[24:25], v[84:85], v[48:49] op_sel_hi:[1,0,0] neg_lo:[0,0,1] neg_hi:[0,0,1]
	v_exp_f32_e32 v24, v24
	v_exp_f32_e32 v25, v25
	v_pk_fma_f32 v[26:27], v[26:27], v[84:85], v[48:49] op_sel_hi:[1,0,0] neg_lo:[0,0,1] neg_hi:[0,0,1]
	v_exp_f32_e32 v26, v26
	v_exp_f32_e32 v27, v27
	v_pk_fma_f32 v[28:29], v[28:29], v[84:85], v[48:49] op_sel_hi:[1,0,0] neg_lo:[0,0,1] neg_hi:[0,0,1]
	v_exp_f32_e32 v28, v28
	v_exp_f32_e32 v29, v29
	v_pk_fma_f32 v[30:31], v[30:31], v[84:85], v[48:49] op_sel_hi:[1,0,0] neg_lo:[0,0,1] neg_hi:[0,0,1]
	v_exp_f32_e32 v30, v30
	v_exp_f32_e32 v31, v31
	v_pk_fma_f32 v[32:33], v[32:33], v[84:85], v[48:49] op_sel_hi:[1,0,0] neg_lo:[0,0,1] neg_hi:[0,0,1]
	v_exp_f32_e32 v32, v32
	v_exp_f32_e32 v33, v33
	v_pk_add_f32 v[56:57], v[18:19], v[20:21]
	v_pk_add_f32 v[58:59], v[22:23], v[24:25]
	v_pk_add_f32 v[60:61], v[26:27], v[28:29]
	v_pk_add_f32 v[62:63], v[30:31], v[32:33]
	v_pk_add_f32 v[56:57], v[56:57], v[58:59]
	v_pk_add_f32 v[60:61], v[60:61], v[62:63]
	v_pk_add_f32 v[56:57], v[56:57], v[60:61]
	v_add_f32_e32 v50, v56, v57
	v_mov_b32_e32 v51, v50
	s_nop 1
	v_permlane32_swap_b32_e32 v50, v51
	v_add_f32_e32 v50, v50, v51
	v_log_f32_e32 v50, v50
	v_cvt_pk_f16_f32 v40, v18, v19
	v_cvt_pk_f16_f32 v41, v20, v21
	v_cvt_pk_f16_f32 v42, v22, v23
	v_cvt_pk_f16_f32 v43, v24, v25
	v_cvt_pk_f16_f32 v44, v26, v27
	v_cvt_pk_f16_f32 v45, v28, v29
	v_cvt_pk_f16_f32 v46, v30, v31
	v_cvt_pk_f16_f32 v47, v32, v33
	v_add_f32_e32 v50, 0x41600000, v50
	v_mul_f32_e32 v50, 0xbf317218, v50
	v_cndmask_b32_e64 v51, v50, 1.0, vcc
	s_waitcnt vmcnt(0)
	ds_read_b128 v[2:5], v39
	ds_read_b128 v[6:9], v81
	ds_read_b128 v[10:13], v82
	ds_read_b128 v[14:17], v83
	s_waitcnt lgkmcnt(2)
	v_max3_f32 v52, v2, v3, v4
	v_max3_f32 v53, v5, v6, v7
	v_max_f32_e32 v52, v52, v8
	v_max_f32_e32 v53, v53, v9
	s_waitcnt lgkmcnt(0)
	v_max3_f32 v52, v52, v10, v11
	v_max3_f32 v53, v53, v12, v13
	v_max3_f32 v52, v52, v14, v15
	v_max3_f32 v53, v53, v16, v17
	v_max_f32_e32 v52, v52, v53
	v_mov_b32_e32 v53, v52
	s_nop 1
	v_permlane32_swap_b32_e32 v52, v53
	v_max_f32_e32 v52, v52, v53
	v_cndmask_b32_e32 v54, 1.0, v52, vcc
	v_fmamk_f32 v48, v52, 0x3fb8aa3b, v34
	v_pk_fma_f32 v[2:3], v[2:3], v[84:85], v[48:49] op_sel_hi:[1,0,0] neg_lo:[0,0,1] neg_hi:[0,0,1]
	v_mfma_f32_32x32x2_f32 v[64:79], v54, v51, 0
	v_exp_f32_e32 v2, v2
	v_exp_f32_e32 v3, v3
	v_pk_fma_f32 v[4:5], v[4:5], v[84:85], v[48:49] op_sel_hi:[1,0,0] neg_lo:[0,0,1] neg_hi:[0,0,1]
	v_exp_f32_e32 v4, v4
	v_exp_f32_e32 v5, v5
	v_pk_fma_f32 v[6:7], v[6:7], v[84:85], v[48:49] op_sel_hi:[1,0,0] neg_lo:[0,0,1] neg_hi:[0,0,1]
	v_exp_f32_e32 v6, v6
	v_exp_f32_e32 v7, v7
	v_pk_fma_f32 v[8:9], v[8:9], v[84:85], v[48:49] op_sel_hi:[1,0,0] neg_lo:[0,0,1] neg_hi:[0,0,1]
	v_exp_f32_e32 v8, v8
	v_exp_f32_e32 v9, v9
	v_pk_fma_f32 v[10:11], v[10:11], v[84:85], v[48:49] op_sel_hi:[1,0,0] neg_lo:[0,0,1] neg_hi:[0,0,1]
	v_exp_f32_e32 v10, v10
	v_cvt_pk_f16_f32 v56, v2, v3
	v_cvt_pk_f16_f32 v57, v4, v5
	v_cvt_pk_f16_f32 v58, v6, v7
	v_cvt_pk_f16_f32 v59, v8, v9
	v_exp_f32_e32 v11, v11
	v_pk_fma_f32 v[12:13], v[12:13], v[84:85], v[48:49] op_sel_hi:[1,0,0] neg_lo:[0,0,1] neg_hi:[0,0,1]
	v_exp_f32_e32 v12, v12
	v_mfma_f32_32x32x16_f16 v[18:33], v[56:59], v[40:43], 0
	v_exp_f32_e32 v13, v13
	v_pk_fma_f32 v[14:15], v[14:15], v[84:85], v[48:49] op_sel_hi:[1,0,0] neg_lo:[0,0,1] neg_hi:[0,0,1]
	v_exp_f32_e32 v14, v14
	v_exp_f32_e32 v15, v15
	v_pk_fma_f32 v[16:17], v[16:17], v[84:85], v[48:49] op_sel_hi:[1,0,0] neg_lo:[0,0,1] neg_hi:[0,0,1]
	v_exp_f32_e32 v16, v16
	v_exp_f32_e32 v17, v17
	v_cvt_pk_f16_f32 v60, v10, v11
	v_cvt_pk_f16_f32 v61, v12, v13
	v_cvt_pk_f16_f32 v62, v14, v15
	v_cvt_pk_f16_f32 v63, v16, v17
	s_nop 1
	v_mfma_f32_32x32x16_f16 v[18:33], v[60:63], v[44:47], v[18:33]
	s_setprio 3
	s_nop 10
	v_log_f32_e32 v18, v18
	v_log_f32_e32 v19, v19
	v_log_f32_e32 v20, v20
	v_log_f32_e32 v21, v21
	v_log_f32_e32 v22, v22
	v_log_f32_e32 v23, v23
	v_pk_fma_f32 v[64:65], v[18:19], v[84:85], v[64:65] op_sel:[0,1,0] op_sel_hi:[1,1,1]
	buffer_store_dword v64, v36, s[8:11], 0 offen
	buffer_store_dword v65, v36, s[8:11], s24 offen
	v_log_f32_e32 v24, v24
	v_log_f32_e32 v25, v25
	v_pk_fma_f32 v[66:67], v[20:21], v[84:85], v[66:67] op_sel:[0,1,0] op_sel_hi:[1,1,1]
	buffer_store_dword v66, v36, s[8:11], s25 offen
	buffer_store_dword v67, v36, s[8:11], s26 offen
	v_log_f32_e32 v26, v26
	v_log_f32_e32 v27, v27
	v_pk_fma_f32 v[68:69], v[22:23], v[84:85], v[68:69] op_sel:[0,1,0] op_sel_hi:[1,1,1]
	buffer_store_dword v68, v36, s[8:11], s27 offen
	buffer_store_dword v69, v36, s[8:11], s28 offen
	v_log_f32_e32 v28, v28
	v_log_f32_e32 v29, v29
	v_pk_fma_f32 v[70:71], v[24:25], v[84:85], v[70:71] op_sel:[0,1,0] op_sel_hi:[1,1,1]
	buffer_store_dword v70, v36, s[8:11], s29 offen
	buffer_store_dword v71, v36, s[8:11], s30 offen
	v_log_f32_e32 v30, v30
	v_log_f32_e32 v31, v31
	v_pk_fma_f32 v[72:73], v[26:27], v[84:85], v[72:73] op_sel:[0,1,0] op_sel_hi:[1,1,1]
	buffer_store_dword v72, v36, s[8:11], s31 offen
	buffer_store_dword v73, v36, s[8:11], s32 offen
	v_log_f32_e32 v32, v32
	v_log_f32_e32 v33, v33
	v_pk_fma_f32 v[74:75], v[28:29], v[84:85], v[74:75] op_sel:[0,1,0] op_sel_hi:[1,1,1]
	buffer_store_dword v74, v36, s[8:11], s33 offen
	buffer_store_dword v75, v36, s[8:11], s34 offen
	v_pk_fma_f32 v[76:77], v[30:31], v[84:85], v[76:77] op_sel:[0,1,0] op_sel_hi:[1,1,1]
	buffer_store_dword v76, v36, s[8:11], s35 offen
	buffer_store_dword v77, v36, s[8:11], s36 offen
	v_pk_fma_f32 v[78:79], v[32:33], v[84:85], v[78:79] op_sel:[0,1,0] op_sel_hi:[1,1,1]
	buffer_store_dword v78, v36, s[8:11], s37 offen
	buffer_store_dword v79, v36, s[8:11], s38 offen
	s_endpgm
